# attention: one batched read of all 8 pool counters when a wave leaves its home pool, so already-exhausted pools are skipped without a failing atomic round trip each
# baseline (speedup 1.0000x reference)
.LBB0_523:
	s_waitcnt lgkmcnt(0)
	s_cmp_le_i32 s94, s4
	s_cselect_b64 s[0:1], -1, 0
	s_cmp_lt_i32 s4, s95
	s_cselect_b64 s[6:7], -1, 0
	s_and_b64 s[0:1], s[0:1], s[6:7]
	s_andn2_b64 vcc, exec, s[0:1]
	s_mov_b64 s[0:1], 0
	v_writelane_b32 v254, s0, 42
	s_mov_b64 s[42:43], 0
	s_nop 0
	v_writelane_b32 v254, s1, 43
	s_cbranch_vccnz .LBB0_602
	s_mov_b64 s[0:1], s[90:91]
	v_mbcnt_lo_u32_b32 v142, -1, 0
	v_mbcnt_hi_u32_b32 v142, -1, v142
	v_readlane_b32 s8, v253, 0
	s_load_dwordx2 s[0:1], s[0:1], 0xb8
	s_waitcnt lgkmcnt(0)
	s_add_u32 s44, s0, 0x24a00000
	s_addc_u32 s45, s1, 0
	s_add_u32 s46, s0, 0x23600000
	s_addc_u32 s47, s1, 0
	s_add_u32 s48, s0, 0x39a00000
	s_addc_u32 s49, s1, 0
	s_add_u32 s50, s0, 0x3a200000
	v_readlane_b32 s4, v254, 37
	s_addc_u32 s51, s1, 0
	s_lshl_b32 s4, s4, 6
	s_lshl_b64 s[6:7], s[4:5], 2
	s_add_u32 s4, s0, s6
	s_addc_u32 s6, s1, s7
	s_add_u32 s4, s4, 0x20000
	s_mulk_i32 s8, 0x4c00
	s_addc_u32 s12, s6, 0
	s_add_i32 s6, s8, 0
	s_waitcnt vmcnt(0)
	v_lshlrev_b32_e32 v1, 4, v142
	v_and_b32_e32 v2, 15, v142
	v_ashrrev_i32_e32 v0, 4, v142
	v_and_b32_e32 v161, 0x70, v1
	v_mov_b32_e32 v1, s6
	v_mad_u32_u24 v3, v2, s3, v1
	v_lshlrev_b32_e32 v5, 2, v0
	v_bfe_u32 v1, v142, 2, 2
	v_or_b32_e32 v6, v5, v1
	v_mul_lo_u32 v1, v6, s3
	v_add_u32_e32 v7, s6, v1
	v_lshlrev_b32_e32 v1, 3, v142
	v_and_b32_e32 v8, 24, v1
	v_lshlrev_b32_e32 v1, 8, v0
	v_lshlrev_b32_e32 v136, 4, v2
	v_lshlrev_b32_e32 v4, 3, v0
	v_add3_u32 v168, s6, v1, v136
	v_lshlrev_b32_e32 v169, 7, v0
	v_lshl_add_u64 v[0:1], s[0:1], 0, v[136:137]
	s_mov_b64 s[0:1], 0x31a00000
	v_ashrrev_i32_e32 v160, 3, v142
	v_lshl_add_u64 v[146:147], v[0:1], 0, s[0:1]
	v_mul_lo_u32 v1, v6, s62
	v_and_b32_e32 v164, -16, v142
	v_add3_u32 v174, s6, v1, v8
	v_mul_u32_u24_e32 v1, 0x120, v2
	v_mul_lo_u32 v176, v160, s3
	v_ashrrev_i32_e32 v143, 31, v142
	v_lshl_add_u32 v165, v160, 1, s6
	v_add_u32_e32 v167, s6, v161
	v_lshlrev_b32_e32 v0, 2, v142
	v_add3_u32 v175, s6, v1, v164
	v_lshlrev_b32_e32 v1, 1, v176
	s_add_i32 s13, s6, 0x4800
	s_getreg_b32 s14, hwreg(HW_REG_XCC_ID, 0, 4)
	s_mov_b32 s15, 0
	v_cmp_eq_u32_e64 s[36:37], 0, v142
	s_add_i32 s28, s6, 0x4a00
	v_lshl_add_u64 v[144:145], v[142:143], 1, s[46:47]
	v_lshl_add_u32 v162, v142, 1, s6
	v_cmp_gt_u32_e64 s[38:39], 4, v2
	v_lshlrev_b32_e32 v163, 7, v2
	v_add_u32_e32 v166, 0x4800, v165
	v_cmp_gt_u32_e64 s[40:41], 16, v142
	v_add_u32_e32 v170, 64, v142
	v_add_u32_e32 v171, 0x80, v142
	v_add_u32_e32 v172, 0xc0, v142
	v_lshl_add_u32 v173, v2, 8, v164
	v_add3_u32 v177, v167, v161, v1
	v_add_u32_e32 v178, 19, v5
	v_add_u32_e32 v179, v3, v4
	v_add_u32_e32 v180, s6, v0
	v_add_u32_e32 v181, v7, v8
	s_movk_i32 s65, 0xff
	s_branch .LBB0_526

.LBB0_526:
	s_add_i32 s10, s15, s14
	s_and_b32 s11, s10, 7
	s_lshl_b32 s0, s11, 12
	s_add_u32 s52, s4, s0
	s_addc_u32 s53, s12, 0
	s_waitcnt vmcnt(16)
	s_cmp_lg_u32 s15, 1
	s_cbranch_scc1 .Lat_nochk
	v_mbcnt_lo_u32_b32 v0, -1, 0
	v_and_b32_e32 v0, 7, v0
	v_lshlrev_b32_e32 v0, 12, v0
	s_mov_b32 s0, s4
	s_mov_b32 s1, s12
	global_load_dword v1, v0, s[0:1] sc1
	s_waitcnt vmcnt(0)
	v_cmp_gt_u32_e32 vcc, 0x2000, v1
	s_and_b32 s65, vcc_lo, 0xff
.Lat_nochk:
	s_bitcmp1_b32 s65, s11
	s_cbranch_scc0 .LBB0_525
	v_mov_b32_e32 v0, 0
	s_and_saveexec_b64 s[0:1], s[36:37]
	s_cbranch_execz .LBB0_530
	s_mov_b64 s[8:9], exec
	v_mbcnt_lo_u32_b32 v0, s8, 0
	v_mbcnt_hi_u32_b32 v0, s9, v0
	v_cmp_eq_u32_e32 vcc, 0, v0
	s_and_saveexec_b64 s[6:7], vcc
	s_cbranch_execz .LBB0_529
	s_bcnt1_i32_b64 s8, s[8:9]
	s_lshl_b32 s8, s8, 2
	v_mov_b32_e32 v1, s8
	global_atomic_add v1, v137, v1, s[52:53] sc0
